# MoE K-loops: rare half-tile drain path moved out of line (common path has no taken branch)
# baseline (speedup 1.0000x reference)
.LBB0_730:
	s_add_i32 s38, s4, 2
	s_cmp_eq_u32 s34, 28
	s_cselect_b64 s[4:5], -1, 0
	s_and_b64 s[34:35], s[4:5], exec
	s_cselect_b32 s38, 0, s38
	s_cselect_b32 s34, s23, s37
	s_cselect_b32 s35, s22, s36
	s_cselect_b32 s66, s21, s25
	s_cselect_b32 s67, s20, s24
	s_cmp_lg_u64 s[2:3], 0
	s_cbranch_scc1 .Lw2_guE
	s_waitcnt vmcnt(4)
.Lwd_guE:
	v_cvt_pk_bf16_f32 v2, v2, v3
	v_cvt_pk_bf16_f32 v3, v4, v5
	s_ashr_i32 s39, s38, 31
	ds_write_b64 v199, v[2:3]
	v_cvt_pk_bf16_f32 v2, v6, v7
	v_cvt_pk_bf16_f32 v3, v8, v9
	s_lshl_b64 s[40:41], s[38:39], 18
	ds_write_b64 v200, v[2:3]
	v_cvt_pk_bf16_f32 v2, v10, v11
	v_cvt_pk_bf16_f32 v3, v12, v13
	s_add_u32 s68, s67, s40
	ds_write_b64 v201, v[2:3]
	v_cvt_pk_bf16_f32 v2, v14, v15
	v_cvt_pk_bf16_f32 v3, v16, v17
	s_addc_u32 s69, s66, s41
	ds_write_b64 v202, v[2:3]
	v_cvt_pk_bf16_f32 v2, v18, v19
	v_cvt_pk_bf16_f32 v3, v20, v21
	s_add_u32 s40, s35, s40
	ds_write_b64 v203, v[2:3]
	v_cvt_pk_bf16_f32 v2, v22, v23
	v_cvt_pk_bf16_f32 v3, v24, v25
	s_addc_u32 s41, s34, s41
	ds_write_b64 v204, v[2:3]
	v_cvt_pk_bf16_f32 v2, v26, v27
	v_cvt_pk_bf16_f32 v3, v28, v29
	s_add_u32 s70, s68, 0x2000
	ds_write_b64 v205, v[2:3]
	v_cvt_pk_bf16_f32 v2, v34, v35
	v_cvt_pk_bf16_f32 v3, v36, v37
	ds_write_b64 v206, v[2:3]
	s_addc_u32 s71, s69, 0
	global_load_dwordx4 v[34:37], v189, s[68:69]
	s_add_u32 s72, s40, 0x2000
	global_load_dwordx4 v[22:25], v189, s[40:41]
	s_addc_u32 s73, s41, 0
	global_load_dwordx4 v[26:29], v189, s[70:71]
	s_add_u32 s70, s68, 0x4000
	s_addc_u32 s71, s69, 0
	global_load_dwordx4 v[14:17], v189, s[72:73]
	s_add_u32 s72, s40, 0x4000
	s_addc_u32 s73, s41, 0
	s_add_u32 s68, s68, 0x6000
	global_load_dwordx4 v[18:21], v189, s[70:71]
	s_addc_u32 s69, s69, 0
	global_load_dwordx4 v[6:9], v189, s[72:73]
	s_add_u32 s40, s40, 0x6000
	s_addc_u32 s41, s41, 0
	global_load_dwordx4 v[10:13], v189, s[68:69]
	global_load_dwordx4 v[2:5], v189, s[40:41]
	s_lshl_b64 s[40:41], s[38:39], 7
	s_add_u32 s40, s8, s40
	s_mov_b32 m0, s51
	s_waitcnt vmcnt(8)
	s_waitcnt lgkmcnt(0)
	s_barrier
	s_addc_u32 s41, s9, s41
	v_cndmask_b32_e64 v164, v178, v209, s[4:5]
	v_cndmask_b32_e64 v163, v180, v210, s[4:5]
	global_load_lds_dwordx4 v164, s[40:41]
	s_mov_b32 m0, s60
	v_cndmask_b32_e64 v162, v213, v208, s[4:5]
	global_load_lds_dwordx4 v163, s[40:41]
	v_cmp_ne_u32_e32 vcc, 0, v162
	s_mov_b64 s[96:97], vcc
	s_cbranch_vccnz .LBB0_732
	v_cndmask_b32_e64 v163, v182, v211, s[4:5]
	s_add_i32 m0, s51, 0x4000
	v_cndmask_b32_e64 v162, v184, v212, s[4:5]
	global_load_lds_dwordx4 v163, s[40:41]
	s_add_i32 m0, s51, 0x6000
	s_nop 0
	global_load_lds_dwordx4 v162, s[40:41]

.LBB0_736:
	s_lshl_b64 s[2:3], s[38:39], 18
	s_add_u32 s4, s2, 0x40000
	s_addc_u32 s5, s3, 0
	s_add_u32 s2, s67, s4
	s_addc_u32 s3, s66, s5
	s_cmp_lg_u64 s[96:97], 0
	s_cbranch_scc1 .Lw2_guO
	s_waitcnt vmcnt(4)
.Lwd_guO:
	v_cvt_pk_bf16_f32 v34, v34, v35
	v_cvt_pk_bf16_f32 v35, v36, v37
	ds_write_b64 v194, v[34:35]
	v_cvt_pk_bf16_f32 v22, v22, v23
	v_cvt_pk_bf16_f32 v23, v24, v25
	s_add_u32 s4, s35, s4
	ds_write_b64 v194, v[22:23] offset:16384
	v_cvt_pk_bf16_f32 v22, v26, v27
	v_cvt_pk_bf16_f32 v23, v28, v29
	ds_write_b64 v195, v[22:23]
	v_cvt_pk_bf16_f32 v14, v14, v15
	v_cvt_pk_bf16_f32 v15, v16, v17
	s_addc_u32 s5, s34, s5
	ds_write_b64 v195, v[14:15] offset:16384
	v_cvt_pk_bf16_f32 v14, v18, v19
	v_cvt_pk_bf16_f32 v15, v20, v21
	ds_write_b64 v196, v[14:15]
	v_cvt_pk_bf16_f32 v6, v6, v7
	v_cvt_pk_bf16_f32 v7, v8, v9
	s_add_u32 s34, s2, 0x2000
	ds_write_b64 v196, v[6:7] offset:16384
	v_cvt_pk_bf16_f32 v6, v10, v11
	v_cvt_pk_bf16_f32 v7, v12, v13
	ds_write_b64 v197, v[6:7]
	v_cvt_pk_bf16_f32 v2, v2, v3
	v_cvt_pk_bf16_f32 v3, v4, v5
	ds_write_b64 v197, v[2:3] offset:16384
	s_addc_u32 s35, s3, 0
	global_load_dwordx4 v[2:5], v189, s[2:3]
	s_add_u32 s38, s4, 0x2000
	global_load_dwordx4 v[6:9], v189, s[4:5]
	s_addc_u32 s39, s5, 0
	global_load_dwordx4 v[10:13], v189, s[34:35]
	s_add_u32 s34, s2, 0x4000
	s_addc_u32 s35, s3, 0
	global_load_dwordx4 v[14:17], v189, s[38:39]
	s_add_u32 s38, s4, 0x4000
	s_addc_u32 s39, s5, 0
	global_load_dwordx4 v[18:21], v189, s[34:35]
	s_add_u32 s2, s2, 0x6000
	global_load_dwordx4 v[22:25], v189, s[38:39]
	s_addc_u32 s3, s3, 0
	s_add_u32 s4, s4, 0x6000
	global_load_dwordx4 v[26:29], v189, s[2:3]
	s_addc_u32 s5, s5, 0
	global_load_dwordx4 v[34:37], v189, s[4:5]
	s_waitcnt vmcnt(8)
	s_waitcnt lgkmcnt(0)
	s_barrier
	s_cmp_gt_u32 s17, 29
	s_cbranch_scc1 .LBB0_738
	s_mov_b32 s34, s17
	s_branch .LBB0_724
.Lw2_guE:
	s_waitcnt vmcnt(2)
	s_branch .Lwd_guE

.LBB0_862:
	s_add_i32 s48, s48, 2
	s_cmp_eq_u32 s35, 12
	s_cselect_b32 s48, 0, s48
	s_cselect_b32 s77, s41, s23
	s_cselect_b32 s82, s40, s22
	s_cselect_b32 s35, s39, s47
	s_cselect_b32 s37, s38, s46
	s_cselect_b32 s43, s27, s45
	s_cselect_b32 s74, s26, s44
	s_cselect_b64 vcc, -1, 0
	s_cmp_lg_u64 s[2:3], 0
	s_cbranch_scc1 .Lw2_dnE
	s_waitcnt vmcnt(4)
.Lwd_dnE:
	v_cvt_pk_bf16_f32 v2, v64, v65
	v_cvt_pk_bf16_f32 v3, v66, v67
	s_ashr_i32 s49, s48, 31
	ds_write_b64 v199, v[2:3]
	v_cvt_pk_bf16_f32 v2, v60, v61
	v_cvt_pk_bf16_f32 v3, v62, v63
	s_lshl_b64 s[50:51], s[48:49], 19
	ds_write_b64 v200, v[2:3]
	v_cvt_pk_bf16_f32 v2, v76, v77
	v_cvt_pk_bf16_f32 v3, v78, v79
	s_add_u32 s72, s74, s50
	ds_write_b64 v201, v[2:3]
	v_cvt_pk_bf16_f32 v2, v72, v73
	v_cvt_pk_bf16_f32 v3, v74, v75
	s_addc_u32 s73, s43, s51
	ds_write_b64 v202, v[2:3]
	v_cvt_pk_bf16_f32 v2, v88, v89
	v_cvt_pk_bf16_f32 v3, v90, v91
	s_add_u32 s50, s37, s50
	ds_write_b64 v203, v[2:3]
	v_cvt_pk_bf16_f32 v2, v84, v85
	v_cvt_pk_bf16_f32 v3, v86, v87
	s_addc_u32 s51, s35, s51
	ds_write_b64 v204, v[2:3]
	v_cvt_pk_bf16_f32 v2, v96, v97
	v_cvt_pk_bf16_f32 v3, v98, v99
	s_add_u32 s78, s72, 0x4000
	ds_write_b64 v205, v[2:3]
	v_cvt_pk_bf16_f32 v2, v92, v93
	v_cvt_pk_bf16_f32 v3, v94, v95
	ds_write_b64 v206, v[2:3]
	s_addc_u32 s79, s73, 0
	global_load_dwordx4 v[96:99], v189, s[72:73]
	s_add_u32 s80, s50, 0x4000
	global_load_dwordx4 v[88:91], v189, s[50:51]
	s_addc_u32 s81, s51, 0
	global_load_dwordx4 v[92:95], v189, s[78:79]
	s_add_u32 s78, s72, 0x8000
	s_addc_u32 s79, s73, 0
	global_load_dwordx4 v[76:79], v189, s[80:81]
	s_add_u32 s80, s50, 0x8000
	s_addc_u32 s81, s51, 0
	s_add_u32 s72, s72, 0xc000
	global_load_dwordx4 v[84:87], v189, s[78:79]
	s_addc_u32 s73, s73, 0
	global_load_dwordx4 v[64:67], v189, s[80:81]
	s_add_u32 s50, s50, 0xc000
	s_addc_u32 s51, s51, 0
	global_load_dwordx4 v[72:75], v189, s[72:73]
	global_load_dwordx4 v[60:63], v189, s[50:51]
	s_lshl_b64 s[50:51], s[48:49], 7
	s_add_u32 s50, s82, s50
	s_addc_u32 s51, s77, s51
	s_mov_b32 m0, s21
	s_waitcnt vmcnt(8)
	s_waitcnt lgkmcnt(0)
	s_barrier
	v_lshl_add_u64 v[2:3], s[50:51], 0, v[180:181]
	global_load_lds_dwordx4 v[2:3], off
	v_lshl_add_u64 v[2:3], s[50:51], 0, v[182:183]
	s_mov_b32 m0, s67
	v_cndmask_b32_e32 v1, v209, v208, vcc
	global_load_lds_dwordx4 v[2:3], off
	v_cmp_ne_u32_e32 vcc, 0, v1
	s_mov_b64 s[96:97], vcc
	s_cbranch_vccnz .LBB0_864
	v_lshl_add_u64 v[164:165], s[50:51], 0, v[184:185]
	s_add_i32 m0, s21, 0x4000
	v_lshl_add_u64 v[2:3], s[50:51], 0, v[186:187]
	global_load_lds_dwordx4 v[164:165], off
	s_add_i32 m0, s21, 0x6000
	s_nop 0
	global_load_lds_dwordx4 v[2:3], off

.LBB0_868:
	s_lshl_b64 s[2:3], s[48:49], 19
	s_cmp_lg_u64 s[96:97], 0
	s_cbranch_scc1 .Lw2_dnO
	s_waitcnt vmcnt(4)
.Lwd_dnO:
	s_add_u32 s48, s2, 0x80000
	v_cvt_pk_bf16_f32 v2, v96, v97
	v_cvt_pk_bf16_f32 v3, v98, v99
	ds_write_b64 v194, v[2:3]
	v_cvt_pk_bf16_f32 v2, v88, v89
	v_cvt_pk_bf16_f32 v3, v90, v91
	s_addc_u32 s49, s3, 0
	ds_write_b64 v194, v[2:3] offset:16384
	v_cvt_pk_bf16_f32 v2, v92, v93
	v_cvt_pk_bf16_f32 v3, v94, v95
	s_add_u32 s2, s74, s48
	ds_write_b64 v195, v[2:3]
	v_cvt_pk_bf16_f32 v2, v76, v77
	v_cvt_pk_bf16_f32 v3, v78, v79
	s_addc_u32 s3, s43, s49
	ds_write_b64 v195, v[2:3] offset:16384
	v_cvt_pk_bf16_f32 v2, v84, v85
	v_cvt_pk_bf16_f32 v3, v86, v87
	s_add_u32 s48, s37, s48
	ds_write_b64 v196, v[2:3]
	v_cvt_pk_bf16_f32 v2, v64, v65
	v_cvt_pk_bf16_f32 v3, v66, v67
	s_addc_u32 s49, s35, s49
	ds_write_b64 v196, v[2:3] offset:16384
	v_cvt_pk_bf16_f32 v2, v72, v73
	v_cvt_pk_bf16_f32 v3, v74, v75
	s_add_u32 s50, s2, 0x4000
	ds_write_b64 v197, v[2:3]
	v_cvt_pk_bf16_f32 v2, v60, v61
	v_cvt_pk_bf16_f32 v3, v62, v63
	ds_write_b64 v197, v[2:3] offset:16384
	s_addc_u32 s51, s3, 0
	global_load_dwordx4 v[64:67], v189, s[2:3]
	s_add_u32 s72, s48, 0x4000
	global_load_dwordx4 v[60:63], v189, s[48:49]
	s_addc_u32 s73, s49, 0
	global_load_dwordx4 v[76:79], v189, s[50:51]
	s_add_u32 s50, s2, 0x8000
	s_addc_u32 s51, s3, 0
	global_load_dwordx4 v[72:75], v189, s[72:73]
	s_add_u32 s72, s48, 0x8000
	s_addc_u32 s73, s49, 0
	global_load_dwordx4 v[88:91], v189, s[50:51]
	s_add_u32 s2, s2, 0xc000
	global_load_dwordx4 v[84:87], v189, s[72:73]
	s_addc_u32 s3, s3, 0
	s_add_u32 s48, s48, 0xc000
	global_load_dwordx4 v[96:99], v189, s[2:3]
	s_addc_u32 s49, s49, 0
	global_load_dwordx4 v[92:95], v189, s[48:49]
	s_waitcnt vmcnt(8)
	s_waitcnt lgkmcnt(0)
	s_barrier
	s_cmp_gt_u32 s34, 13
	s_cbranch_scc1 .LBB0_870
	s_mov_b32 s35, s34
	s_branch .LBB0_856
